# speedup vs baseline: 1.4224x; 1.1308x over previous
_Z11edge_kernelILi64ELb0EEvPKfS1_PKDF16_PKiS5_S1_S1_S1_S1_S1_PDF16_:
	s_load_dwordx16 s[4:19], s[0:1], 0x10
	s_load_dwordx2 s[20:21], s[0:1], 0x50
	v_readfirstlane_b32 s3, v0
	v_bfe_u32 v139, v0, 4, 2
	v_and_b32_e32 v140, 15, v0
	v_and_b32_e32 v142, 63, v0
	s_lshr_b32 s3, s3, 6
	s_lshl_b32 s2, s2, 1
	s_add_i32 s2, s2, s3
	v_lshlrev_b32_e32 v138, 8, v139
	v_lshl_or_b32 v138, v140, 4, v138
	v_lshlrev_b32_e32 v143, 4, v142
	v_lshl_or_b32 v141, v140, 2, v139
	v_lshlrev_b32_e32 v141, 2, v141
	v_lshlrev_b32_e32 v142, 5, v139
	v_lshlrev_b32_e32 v137, 12, v139
	v_lshl_or_b32 v137, v140, 4, v137
	s_lshl_b32 s28, s2, 14
	s_lshl_b32 s29, s2, 14
	s_lshl_b32 s30, s2, 2
	s_lshl_b32 s31, s2, 8
	s_lshl_b32 s33, s3, 10
	s_lshl_b32 s34, s3, 8
	s_addk_i32 s34, 0x4000
	s_waitcnt lgkmcnt(0)
	s_add_u32 s6, s6, s30
	s_addc_u32 s7, s7, 0
	s_add_u32 s8, s8, s30
	s_addc_u32 s9, s9, 0
	s_load_dword s35, s[6:7], 0x0
	s_load_dword s36, s[8:9], 0x0
	s_add_u32 s10, s10, s28
	s_addc_u32 s11, s11, 0
	s_add_u32 s18, s18, s33
	s_addc_u32 s19, s19, 0
	s_mov_b32 m0, s33
	s_add_u32 s14, s14, s29
	s_addc_u32 s15, s15, 0
	global_load_lds_dwordx4 v143, s[18:19]
	global_load_lds_dwordx4 v143, s[18:19] offset:2048
	s_add_u32 m0, m0, 0x1000
	s_add_u32 s18, s18, 0x1000
	s_addc_u32 s19, s19, 0
	global_load_lds_dwordx4 v143, s[18:19]
	global_load_lds_dwordx4 v143, s[18:19] offset:2048
	s_add_u32 m0, m0, 0x1000
	s_add_u32 s18, s18, 0x1000
	s_addc_u32 s19, s19, 0
	global_load_lds_dwordx4 v143, s[18:19]
	global_load_lds_dwordx4 v143, s[18:19] offset:2048
	s_add_u32 m0, m0, 0x1000
	s_add_u32 s18, s18, 0x1000
	s_addc_u32 s19, s19, 0
	global_load_lds_dwordx4 v143, s[18:19]
	global_load_lds_dwordx4 v143, s[18:19] offset:2048
	s_add_u32 s12, s12, s31
	s_addc_u32 s13, s13, 0
	s_add_u32 s16, s16, s31
	s_addc_u32 s17, s17, 0
	s_waitcnt lgkmcnt(0)
	s_lshl_b32 s36, s36, 7
	s_add_u32 s20, s20, s36
	s_addc_u32 s21, s21, 0
	s_lshl_b32 s37, s35, 7
	s_add_u32 s4, s4, s37
	s_addc_u32 s5, s5, 0
	global_load_dwordx4 v[128:131], v142, s[4:5] nt
	global_load_dwordx4 v[132:135], v142, s[4:5] offset:16 nt
	global_load_dword v136, v141, s[12:13] nt
	global_load_dword v137, v141, s[16:17] nt
	v_add_u32_e32 v142, s34, v141
	v_lshl_add_u32 v143, v139, 2, s34
	s_waitcnt vmcnt(2)
	s_barrier
	v_cvt_f32_f16_e32 v144, v128
	v_cvt_f32_f16_sdwa v145, v128 dst_sel:DWORD dst_unused:UNUSED_PAD src0_sel:WORD_1
	v_cvt_f32_f16_e32 v146, v129
	v_cvt_f32_f16_sdwa v147, v129 dst_sel:DWORD dst_unused:UNUSED_PAD src0_sel:WORD_1
	v_cvt_f32_f16_e32 v148, v130
	v_cvt_f32_f16_sdwa v149, v130 dst_sel:DWORD dst_unused:UNUSED_PAD src0_sel:WORD_1
	v_cvt_f32_f16_e32 v150, v131
	v_cvt_f32_f16_sdwa v151, v131 dst_sel:DWORD dst_unused:UNUSED_PAD src0_sel:WORD_1
	v_cvt_f32_f16_e32 v152, v132
	v_cvt_f32_f16_sdwa v153, v132 dst_sel:DWORD dst_unused:UNUSED_PAD src0_sel:WORD_1
	v_cvt_f32_f16_e32 v154, v133
	v_cvt_f32_f16_sdwa v155, v133 dst_sel:DWORD dst_unused:UNUSED_PAD src0_sel:WORD_1
	v_cvt_f32_f16_e32 v156, v134
	v_cvt_f32_f16_sdwa v157, v134 dst_sel:DWORD dst_unused:UNUSED_PAD src0_sel:WORD_1
	v_cvt_f32_f16_e32 v158, v135
	v_cvt_f32_f16_sdwa v159, v135 dst_sel:DWORD dst_unused:UNUSED_PAD src0_sel:WORD_1
	v_max_f32_e32 v144, 0, v144
	v_max_f32_e32 v145, 0, v145
	v_max_f32_e32 v146, 0, v146
	v_max_f32_e32 v147, 0, v147
	v_max_f32_e32 v148, 0, v148
	v_max_f32_e32 v149, 0, v149
	v_max_f32_e32 v150, 0, v150
	v_max_f32_e32 v151, 0, v151
	v_max_f32_e32 v152, 0, v152
	v_max_f32_e32 v153, 0, v153
	v_max_f32_e32 v154, 0, v154
	v_max_f32_e32 v155, 0, v155
	v_max_f32_e32 v156, 0, v156
	v_max_f32_e32 v157, 0, v157
	v_max_f32_e32 v158, 0, v158
	v_max_f32_e32 v159, 0, v159
	v_cmp_neq_f32_e64 s[40:41], 0, v144
	v_cmp_neq_f32_e64 s[42:43], 0, v145
	v_cmp_neq_f32_e64 s[44:45], 0, v146
	v_cmp_neq_f32_e64 s[46:47], 0, v147
	v_cmp_neq_f32_e64 s[48:49], 0, v148
	v_cmp_neq_f32_e64 s[50:51], 0, v149
	v_cmp_neq_f32_e64 s[52:53], 0, v150
	v_cmp_neq_f32_e64 s[54:55], 0, v151
	v_cmp_neq_f32_e64 s[56:57], 0, v152
	v_cmp_neq_f32_e64 s[58:59], 0, v153
	v_cmp_neq_f32_e64 s[60:61], 0, v154
	v_cmp_neq_f32_e64 s[62:63], 0, v155
	v_cmp_neq_f32_e64 s[64:65], 0, v156
	v_cmp_neq_f32_e64 s[66:67], 0, v157
	v_cmp_neq_f32_e64 s[68:69], 0, v158
	v_cmp_neq_f32_e64 s[70:71], 0, v159
	v_lshlrev_b32_e32 v160, 12, v139
	v_lshl_or_b32 v160, v140, 4, v160
	s_mov_b64 exec, s[40:41]
	global_load_dwordx4 v[0:3], v160, s[10:11] nt
	s_mov_b64 exec, s[42:43]
	global_load_dwordx4 v[4:7], v160, s[10:11] offset:256 nt
	s_mov_b64 exec, s[44:45]
	global_load_dwordx4 v[8:11], v160, s[10:11] offset:512 nt
	s_mov_b64 exec, s[46:47]
	global_load_dwordx4 v[12:15], v160, s[10:11] offset:768 nt
	s_mov_b64 exec, s[48:49]
	global_load_dwordx4 v[16:19], v160, s[10:11] offset:1024 nt
	s_mov_b64 exec, s[50:51]
	global_load_dwordx4 v[20:23], v160, s[10:11] offset:1280 nt
	s_mov_b64 exec, s[52:53]
	global_load_dwordx4 v[24:27], v160, s[10:11] offset:1536 nt
	s_mov_b64 exec, s[54:55]
	global_load_dwordx4 v[28:31], v160, s[10:11] offset:1792 nt
	s_mov_b64 exec, s[56:57]
	global_load_dwordx4 v[32:35], v160, s[10:11] offset:2048 nt
	s_mov_b64 exec, s[58:59]
	global_load_dwordx4 v[36:39], v160, s[10:11] offset:2304 nt
	s_mov_b64 exec, s[60:61]
	global_load_dwordx4 v[40:43], v160, s[10:11] offset:2560 nt
	s_mov_b64 exec, s[62:63]
	global_load_dwordx4 v[44:47], v160, s[10:11] offset:2816 nt
	s_mov_b64 exec, s[64:65]
	global_load_dwordx4 v[48:51], v160, s[10:11] offset:3072 nt
	s_mov_b64 exec, s[66:67]
	global_load_dwordx4 v[52:55], v160, s[10:11] offset:3328 nt
	s_mov_b64 exec, s[68:69]
	global_load_dwordx4 v[56:59], v160, s[10:11] offset:3584 nt
	s_mov_b64 exec, s[70:71]
	global_load_dwordx4 v[60:63], v160, s[10:11] offset:3840 nt
	s_mov_b64 exec, -1
	v_mov_b32_e32 v160, 0
	v_mov_b32_e32 v161, 0
	v_mov_b32_e32 v162, 0
	v_mov_b32_e32 v163, 0
	v_mov_b32_e32 v164, 0
	v_mov_b32_e32 v165, 0
	v_mov_b32_e32 v166, 0
	v_mov_b32_e32 v167, 0
	s_waitcnt vmcnt(0)
	s_mov_b64 exec, s[40:41]
	v_pk_fma_f32 v[160:161], v[144:145], v[0:1], v[160:161] op_sel_hi:[0,1,1]
	v_pk_fma_f32 v[162:163], v[144:145], v[2:3], v[162:163] op_sel_hi:[0,1,1]
	s_mov_b64 exec, s[42:43]
	v_pk_fma_f32 v[164:165], v[144:145], v[4:5], v[164:165] op_sel:[1,0,0]
	v_pk_fma_f32 v[166:167], v[144:145], v[6:7], v[166:167] op_sel:[1,0,0]
	s_mov_b64 exec, s[44:45]
	v_pk_fma_f32 v[160:161], v[146:147], v[8:9], v[160:161] op_sel_hi:[0,1,1]
	v_pk_fma_f32 v[162:163], v[146:147], v[10:11], v[162:163] op_sel_hi:[0,1,1]
	s_mov_b64 exec, s[46:47]
	v_pk_fma_f32 v[164:165], v[146:147], v[12:13], v[164:165] op_sel:[1,0,0]
	v_pk_fma_f32 v[166:167], v[146:147], v[14:15], v[166:167] op_sel:[1,0,0]
	s_mov_b64 exec, s[48:49]
	v_pk_fma_f32 v[160:161], v[148:149], v[16:17], v[160:161] op_sel_hi:[0,1,1]
	v_pk_fma_f32 v[162:163], v[148:149], v[18:19], v[162:163] op_sel_hi:[0,1,1]
	s_mov_b64 exec, s[50:51]
	v_pk_fma_f32 v[164:165], v[148:149], v[20:21], v[164:165] op_sel:[1,0,0]
	v_pk_fma_f32 v[166:167], v[148:149], v[22:23], v[166:167] op_sel:[1,0,0]
	s_mov_b64 exec, s[52:53]
	v_pk_fma_f32 v[160:161], v[150:151], v[24:25], v[160:161] op_sel_hi:[0,1,1]
	v_pk_fma_f32 v[162:163], v[150:151], v[26:27], v[162:163] op_sel_hi:[0,1,1]
	s_mov_b64 exec, s[54:55]
	v_pk_fma_f32 v[164:165], v[150:151], v[28:29], v[164:165] op_sel:[1,0,0]
	v_pk_fma_f32 v[166:167], v[150:151], v[30:31], v[166:167] op_sel:[1,0,0]
	s_mov_b64 exec, s[56:57]
	v_pk_fma_f32 v[160:161], v[152:153], v[32:33], v[160:161] op_sel_hi:[0,1,1]
	v_pk_fma_f32 v[162:163], v[152:153], v[34:35], v[162:163] op_sel_hi:[0,1,1]
	s_mov_b64 exec, s[58:59]
	v_pk_fma_f32 v[164:165], v[152:153], v[36:37], v[164:165] op_sel:[1,0,0]
	v_pk_fma_f32 v[166:167], v[152:153], v[38:39], v[166:167] op_sel:[1,0,0]
	s_mov_b64 exec, s[60:61]
	v_pk_fma_f32 v[160:161], v[154:155], v[40:41], v[160:161] op_sel_hi:[0,1,1]
	v_pk_fma_f32 v[162:163], v[154:155], v[42:43], v[162:163] op_sel_hi:[0,1,1]
	s_mov_b64 exec, s[62:63]
	v_pk_fma_f32 v[164:165], v[154:155], v[44:45], v[164:165] op_sel:[1,0,0]
	v_pk_fma_f32 v[166:167], v[154:155], v[46:47], v[166:167] op_sel:[1,0,0]
	s_mov_b64 exec, s[64:65]
	v_pk_fma_f32 v[160:161], v[156:157], v[48:49], v[160:161] op_sel_hi:[0,1,1]
	v_pk_fma_f32 v[162:163], v[156:157], v[50:51], v[162:163] op_sel_hi:[0,1,1]
	s_mov_b64 exec, s[66:67]
	v_pk_fma_f32 v[164:165], v[156:157], v[52:53], v[164:165] op_sel:[1,0,0]
	v_pk_fma_f32 v[166:167], v[156:157], v[54:55], v[166:167] op_sel:[1,0,0]
	s_mov_b64 exec, s[68:69]
	v_pk_fma_f32 v[160:161], v[158:159], v[56:57], v[160:161] op_sel_hi:[0,1,1]
	v_pk_fma_f32 v[162:163], v[158:159], v[58:59], v[162:163] op_sel_hi:[0,1,1]
	s_mov_b64 exec, s[70:71]
	v_pk_fma_f32 v[164:165], v[158:159], v[60:61], v[164:165] op_sel:[1,0,0]
	v_pk_fma_f32 v[166:167], v[158:159], v[62:63], v[166:167] op_sel:[1,0,0]
	s_mov_b64 exec, -1
	v_pk_add_f32 v[160:161], v[160:161], v[164:165]
	v_pk_add_f32 v[162:163], v[162:163], v[166:167]
	s_nop 1
	v_permlane16_swap_b32_e32 v160, v161
	v_permlane16_swap_b32_e32 v162, v163
	v_add_f32_e32 v160, v160, v161
	v_add_f32_e32 v162, v162, v163
	s_nop 1
	v_permlane32_swap_b32_e32 v160, v162
	v_add_f32_e32 v160, v160, v162
	s_waitcnt vmcnt(17)
	v_add_f32_e32 v160, v160, v136
	v_max_f32_e32 v160, 0, v160
	ds_write_b32 v142, v160
	ds_read2_b32 v[144:145], v143 offset0:0 offset1:4
	ds_read2_b32 v[146:147], v143 offset0:8 offset1:12
	ds_read2_b32 v[148:149], v143 offset0:16 offset1:20
	ds_read2_b32 v[150:151], v143 offset0:24 offset1:28
	ds_read2_b32 v[152:153], v143 offset0:32 offset1:36
	ds_read2_b32 v[154:155], v143 offset0:40 offset1:44
	ds_read2_b32 v[156:157], v143 offset0:48 offset1:52
	ds_read2_b32 v[158:159], v143 offset0:56 offset1:60
	ds_read_b128 v[0:3], v138
	ds_read_b128 v[4:7], v138 offset:1024
	ds_read_b128 v[8:11], v138 offset:2048
	ds_read_b128 v[12:15], v138 offset:3072
	ds_read_b128 v[16:19], v138 offset:4096
	ds_read_b128 v[20:23], v138 offset:5120
	s_waitcnt lgkmcnt(6)
	v_cmp_neq_f32_e64 s[40:41], 0, v144
	v_cmp_neq_f32_e64 s[42:43], 0, v145
	v_cmp_neq_f32_e64 s[44:45], 0, v146
	v_cmp_neq_f32_e64 s[46:47], 0, v147
	v_cmp_neq_f32_e64 s[48:49], 0, v148
	v_cmp_neq_f32_e64 s[50:51], 0, v149
	v_cmp_neq_f32_e64 s[52:53], 0, v150
	v_cmp_neq_f32_e64 s[54:55], 0, v151
	v_cmp_neq_f32_e64 s[56:57], 0, v152
	v_cmp_neq_f32_e64 s[58:59], 0, v153
	v_cmp_neq_f32_e64 s[60:61], 0, v154
	v_cmp_neq_f32_e64 s[62:63], 0, v155
	v_cmp_neq_f32_e64 s[64:65], 0, v156
	v_cmp_neq_f32_e64 s[66:67], 0, v157
	v_cmp_neq_f32_e64 s[68:69], 0, v158
	v_cmp_neq_f32_e64 s[70:71], 0, v159
	s_mov_b64 exec, s[40:41]
	global_load_dwordx4 v[64:67], v138, s[14:15] nt
	s_mov_b64 exec, s[42:43]
	global_load_dwordx4 v[68:71], v138, s[14:15] offset:1024 nt
	s_mov_b64 exec, s[44:45]
	global_load_dwordx4 v[72:75], v138, s[14:15] offset:2048 nt
	s_mov_b64 exec, s[46:47]
	global_load_dwordx4 v[76:79], v138, s[14:15] offset:3072 nt
	s_add_u32 s14, s14, 0x1000
	s_addc_u32 s15, s15, 0
	s_mov_b64 exec, s[48:49]
	global_load_dwordx4 v[80:83], v138, s[14:15] nt
	s_mov_b64 exec, s[50:51]
	global_load_dwordx4 v[84:87], v138, s[14:15] offset:1024 nt
	s_mov_b64 exec, s[52:53]
	global_load_dwordx4 v[88:91], v138, s[14:15] offset:2048 nt
	s_mov_b64 exec, s[54:55]
	global_load_dwordx4 v[92:95], v138, s[14:15] offset:3072 nt
	s_add_u32 s14, s14, 0x1000
	s_addc_u32 s15, s15, 0
	s_mov_b64 exec, s[56:57]
	global_load_dwordx4 v[96:99], v138, s[14:15] nt
	s_mov_b64 exec, s[58:59]
	global_load_dwordx4 v[100:103], v138, s[14:15] offset:1024 nt
	s_mov_b64 exec, s[60:61]
	global_load_dwordx4 v[104:107], v138, s[14:15] offset:2048 nt
	s_mov_b64 exec, s[62:63]
	global_load_dwordx4 v[108:111], v138, s[14:15] offset:3072 nt
	s_add_u32 s14, s14, 0x1000
	s_addc_u32 s15, s15, 0
	s_mov_b64 exec, s[64:65]
	global_load_dwordx4 v[112:115], v138, s[14:15] nt
	s_mov_b64 exec, s[66:67]
	global_load_dwordx4 v[116:119], v138, s[14:15] offset:1024 nt
	s_mov_b64 exec, s[68:69]
	global_load_dwordx4 v[120:123], v138, s[14:15] offset:2048 nt
	s_mov_b64 exec, s[70:71]
	global_load_dwordx4 v[124:127], v138, s[14:15] offset:3072 nt
	s_mov_b64 exec, -1
	v_mov_b32_e32 v160, 0
	v_mov_b32_e32 v161, 0
	v_mov_b32_e32 v162, 0
	v_mov_b32_e32 v163, 0
	v_mov_b32_e32 v164, 0
	v_mov_b32_e32 v165, 0
	v_mov_b32_e32 v166, 0
	v_mov_b32_e32 v167, 0
	s_waitcnt lgkmcnt(0)
	ds_read_b128 v[24:27], v138 offset:6144
	ds_read_b128 v[28:31], v138 offset:7168
	ds_read_b128 v[32:35], v138 offset:8192
	ds_read_b128 v[36:39], v138 offset:9216
	ds_read_b128 v[40:43], v138 offset:10240
	ds_read_b128 v[44:47], v138 offset:11264
	ds_read_b128 v[48:51], v138 offset:12288
	ds_read_b128 v[52:55], v138 offset:13312
	ds_read_b128 v[56:59], v138 offset:14336
	ds_read_b128 v[60:63], v138 offset:15360
	s_waitcnt vmcnt(0)
	s_mov_b64 exec, s[40:41]
	v_pk_fma_f32 v[160:161], v[144:145], v[64:65], v[160:161] op_sel_hi:[0,1,1]
	v_pk_fma_f32 v[162:163], v[144:145], v[66:67], v[162:163] op_sel_hi:[0,1,1]
	s_mov_b64 exec, s[42:43]
	v_pk_fma_f32 v[164:165], v[144:145], v[68:69], v[164:165] op_sel:[1,0,0]
	v_pk_fma_f32 v[166:167], v[144:145], v[70:71], v[166:167] op_sel:[1,0,0]
	s_mov_b64 exec, s[44:45]
	v_pk_fma_f32 v[160:161], v[146:147], v[72:73], v[160:161] op_sel_hi:[0,1,1]
	v_pk_fma_f32 v[162:163], v[146:147], v[74:75], v[162:163] op_sel_hi:[0,1,1]
	s_mov_b64 exec, s[46:47]
	v_pk_fma_f32 v[164:165], v[146:147], v[76:77], v[164:165] op_sel:[1,0,0]
	v_pk_fma_f32 v[166:167], v[146:147], v[78:79], v[166:167] op_sel:[1,0,0]
	s_mov_b64 exec, s[48:49]
	v_pk_fma_f32 v[160:161], v[148:149], v[80:81], v[160:161] op_sel_hi:[0,1,1]
	v_pk_fma_f32 v[162:163], v[148:149], v[82:83], v[162:163] op_sel_hi:[0,1,1]
	s_mov_b64 exec, s[50:51]
	v_pk_fma_f32 v[164:165], v[148:149], v[84:85], v[164:165] op_sel:[1,0,0]
	v_pk_fma_f32 v[166:167], v[148:149], v[86:87], v[166:167] op_sel:[1,0,0]
	s_mov_b64 exec, s[52:53]
	v_pk_fma_f32 v[160:161], v[150:151], v[88:89], v[160:161] op_sel_hi:[0,1,1]
	v_pk_fma_f32 v[162:163], v[150:151], v[90:91], v[162:163] op_sel_hi:[0,1,1]
	s_mov_b64 exec, s[54:55]
	v_pk_fma_f32 v[164:165], v[150:151], v[92:93], v[164:165] op_sel:[1,0,0]
	v_pk_fma_f32 v[166:167], v[150:151], v[94:95], v[166:167] op_sel:[1,0,0]
	s_mov_b64 exec, s[56:57]
	v_pk_fma_f32 v[160:161], v[152:153], v[96:97], v[160:161] op_sel_hi:[0,1,1]
	v_pk_fma_f32 v[162:163], v[152:153], v[98:99], v[162:163] op_sel_hi:[0,1,1]
	s_mov_b64 exec, s[58:59]
	v_pk_fma_f32 v[164:165], v[152:153], v[100:101], v[164:165] op_sel:[1,0,0]
	v_pk_fma_f32 v[166:167], v[152:153], v[102:103], v[166:167] op_sel:[1,0,0]
	s_mov_b64 exec, s[60:61]
	v_pk_fma_f32 v[160:161], v[154:155], v[104:105], v[160:161] op_sel_hi:[0,1,1]
	v_pk_fma_f32 v[162:163], v[154:155], v[106:107], v[162:163] op_sel_hi:[0,1,1]
	s_mov_b64 exec, s[62:63]
	v_pk_fma_f32 v[164:165], v[154:155], v[108:109], v[164:165] op_sel:[1,0,0]
	v_pk_fma_f32 v[166:167], v[154:155], v[110:111], v[166:167] op_sel:[1,0,0]
	s_mov_b64 exec, s[64:65]
	v_pk_fma_f32 v[160:161], v[156:157], v[112:113], v[160:161] op_sel_hi:[0,1,1]
	v_pk_fma_f32 v[162:163], v[156:157], v[114:115], v[162:163] op_sel_hi:[0,1,1]
	s_mov_b64 exec, s[66:67]
	v_pk_fma_f32 v[164:165], v[156:157], v[116:117], v[164:165] op_sel:[1,0,0]
	v_pk_fma_f32 v[166:167], v[156:157], v[118:119], v[166:167] op_sel:[1,0,0]
	s_mov_b64 exec, s[68:69]
	v_pk_fma_f32 v[160:161], v[158:159], v[120:121], v[160:161] op_sel_hi:[0,1,1]
	v_pk_fma_f32 v[162:163], v[158:159], v[122:123], v[162:163] op_sel_hi:[0,1,1]
	s_mov_b64 exec, s[70:71]
	v_pk_fma_f32 v[164:165], v[158:159], v[124:125], v[164:165] op_sel:[1,0,0]
	v_pk_fma_f32 v[166:167], v[158:159], v[126:127], v[166:167] op_sel:[1,0,0]
	s_mov_b64 exec, -1
	v_pk_add_f32 v[160:161], v[160:161], v[164:165]
	v_pk_add_f32 v[162:163], v[162:163], v[166:167]
	s_nop 1
	v_permlane16_swap_b32_e32 v160, v161
	v_permlane16_swap_b32_e32 v162, v163
	v_add_f32_e32 v160, v160, v161
	v_add_f32_e32 v162, v162, v163
	s_nop 1
	v_permlane32_swap_b32_e32 v160, v162
	v_add_f32_e32 v160, v160, v162
	v_add_f32_e32 v160, v160, v137
	s_waitcnt lgkmcnt(0)
	ds_write_b32 v142, v160
	ds_read2_b32 v[144:145], v143 offset0:0 offset1:4
	ds_read2_b32 v[146:147], v143 offset0:8 offset1:12
	ds_read2_b32 v[148:149], v143 offset0:16 offset1:20
	ds_read2_b32 v[150:151], v143 offset0:24 offset1:28
	ds_read2_b32 v[152:153], v143 offset0:32 offset1:36
	ds_read2_b32 v[154:155], v143 offset0:40 offset1:44
	ds_read2_b32 v[156:157], v143 offset0:48 offset1:52
	ds_read2_b32 v[158:159], v143 offset0:56 offset1:60
	v_lshlrev_b32_e32 v136, 3, v140
	v_lshl_or_b32 v136, v139, 2, v136
	v_cmp_gt_u32_e32 vcc, 2, v139
	s_waitcnt lgkmcnt(0)
	v_pk_mul_f32 v[160:161], v[144:145], v[0:1] op_sel_hi:[0,1]
	v_pk_mul_f32 v[162:163], v[144:145], v[2:3] op_sel_hi:[0,1]
	v_pk_mul_f32 v[164:165], v[144:145], v[4:5] op_sel:[1,0]
	v_pk_mul_f32 v[166:167], v[144:145], v[6:7] op_sel:[1,0]
	v_pk_fma_f32 v[160:161], v[146:147], v[8:9], v[160:161] op_sel_hi:[0,1,1]
	v_pk_fma_f32 v[162:163], v[146:147], v[10:11], v[162:163] op_sel_hi:[0,1,1]
	v_pk_fma_f32 v[164:165], v[146:147], v[12:13], v[164:165] op_sel:[1,0,0]
	v_pk_fma_f32 v[166:167], v[146:147], v[14:15], v[166:167] op_sel:[1,0,0]
	v_pk_fma_f32 v[160:161], v[148:149], v[16:17], v[160:161] op_sel_hi:[0,1,1]
	v_pk_fma_f32 v[162:163], v[148:149], v[18:19], v[162:163] op_sel_hi:[0,1,1]
	v_pk_fma_f32 v[164:165], v[148:149], v[20:21], v[164:165] op_sel:[1,0,0]
	v_pk_fma_f32 v[166:167], v[148:149], v[22:23], v[166:167] op_sel:[1,0,0]
	v_pk_fma_f32 v[160:161], v[150:151], v[24:25], v[160:161] op_sel_hi:[0,1,1]
	v_pk_fma_f32 v[162:163], v[150:151], v[26:27], v[162:163] op_sel_hi:[0,1,1]
	v_pk_fma_f32 v[164:165], v[150:151], v[28:29], v[164:165] op_sel:[1,0,0]
	v_pk_fma_f32 v[166:167], v[150:151], v[30:31], v[166:167] op_sel:[1,0,0]
	v_pk_fma_f32 v[160:161], v[152:153], v[32:33], v[160:161] op_sel_hi:[0,1,1]
	v_pk_fma_f32 v[162:163], v[152:153], v[34:35], v[162:163] op_sel_hi:[0,1,1]
	v_pk_fma_f32 v[164:165], v[152:153], v[36:37], v[164:165] op_sel:[1,0,0]
	v_pk_fma_f32 v[166:167], v[152:153], v[38:39], v[166:167] op_sel:[1,0,0]
	v_pk_fma_f32 v[160:161], v[154:155], v[40:41], v[160:161] op_sel_hi:[0,1,1]
	v_pk_fma_f32 v[162:163], v[154:155], v[42:43], v[162:163] op_sel_hi:[0,1,1]
	v_pk_fma_f32 v[164:165], v[154:155], v[44:45], v[164:165] op_sel:[1,0,0]
	v_pk_fma_f32 v[166:167], v[154:155], v[46:47], v[166:167] op_sel:[1,0,0]
	v_pk_fma_f32 v[160:161], v[156:157], v[48:49], v[160:161] op_sel_hi:[0,1,1]
	v_pk_fma_f32 v[162:163], v[156:157], v[50:51], v[162:163] op_sel_hi:[0,1,1]
	v_pk_fma_f32 v[164:165], v[156:157], v[52:53], v[164:165] op_sel:[1,0,0]
	v_pk_fma_f32 v[166:167], v[156:157], v[54:55], v[166:167] op_sel:[1,0,0]
	v_pk_fma_f32 v[160:161], v[158:159], v[56:57], v[160:161] op_sel_hi:[0,1,1]
	v_pk_fma_f32 v[162:163], v[158:159], v[58:59], v[162:163] op_sel_hi:[0,1,1]
	v_pk_fma_f32 v[164:165], v[158:159], v[60:61], v[164:165] op_sel:[1,0,0]
	v_pk_fma_f32 v[166:167], v[158:159], v[62:63], v[166:167] op_sel:[1,0,0]
	v_pk_add_f32 v[160:161], v[160:161], v[164:165]
	v_pk_add_f32 v[162:163], v[162:163], v[166:167]
	s_nop 1
	v_permlane16_swap_b32_e32 v160, v162
	v_permlane16_swap_b32_e32 v161, v163
	v_add_f32_e32 v160, v160, v162
	v_add_f32_e32 v161, v161, v163
	v_mov_b32_e32 v144, v160
	v_mov_b32_e32 v145, v161
	s_nop 1
	v_permlane32_swap_b32_e32 v160, v144
	v_permlane32_swap_b32_e32 v161, v145
	v_add_f32_e32 v160, v160, v144
	v_add_f32_e32 v161, v161, v145
	v_cvt_pk_f16_f32 v137, v160, v161
	s_and_saveexec_b64 s[4:5], vcc
	global_atomic_pk_add_f16 v136, v137, s[20:21]
	s_endpgm
	.p2align	8
